# speedup vs baseline: 1.0141x; 1.0141x over previous
.LBB1_29:
	s_add_i32 s20, s26, 1
	s_and_b64 s[2:3], s[18:19], exec
	s_cselect_b32 s2, s27, s20
	s_lshl_b32 s4, s2, 12
	s_waitcnt vmcnt(6)
	v_lshl_add_u64 v[72:73], v[100:101], 0, s[4:5]
	s_and_saveexec_b64 s[44:45], s[8:9]
	s_and_b64 exec, exec, s[18:19]
	global_load_dwordx4 v[92:95], v[72:73], off
	global_load_dwordx4 v[80:83], v[72:73], off offset:1024
	global_load_dwordx4 v[88:91], v[72:73], off offset:2048
	global_load_dwordx4 v[84:87], v[72:73], off offset:3072
	s_mov_b64 exec, s[44:45]
	s_add_i32 s2, s26, 3
	s_cmp_lt_u32 s26, 17
	s_cselect_b32 s2, s2, s20
	s_lshl_b32 s4, s2, 11
	s_lshl_b64 s[2:3], s[4:5], 2
	v_lshl_add_u64 v[72:73], v[96:97], 0, s[2:3]
	v_lshl_add_u64 v[74:75], v[98:99], 0, s[2:3]
	s_and_saveexec_b64 s[44:45], s[18:19]
	global_load_dwordx4 v[76:79], v[72:73], off nt
	s_and_b64 exec, exec, s[0:1]
	global_load_dwordx4 v[72:75], v[74:75], off nt
	s_mov_b64 exec, s[44:45]
	v_lshl_add_u64 v[102:103], v[102:103], 0, s[14:15]
	s_mov_b32 s26, s27
	s_and_b64 vcc, exec, s[16:17]
	s_cbranch_vccz .LBB1_7
